# instruction-stream L2 prefetch: at each grid-barrier arrival idle waves 4..7 touch the next 32 KiB of code (one dword per 128B line)
# speedup vs baseline: 1.0038x; 1.0038x over previous
.LBB0_90:
	s_cmp_lt_i32 s28, 2
	s_cselect_b64 s[0:1], -1, 0
	s_cmp_gt_i32 s29, 2
	s_cselect_b64 s[4:5], -1, 0
	s_and_b64 s[0:1], s[0:1], s[4:5]
	s_andn2_b64 vcc, exec, s[0:1]
	s_cbranch_vccnz .LBB0_240
	s_waitcnt vmcnt(0)
	s_barrier
	s_cmp_lt_u32 s98, 4
	s_cbranch_scc1 .Lipf_skip_0
	s_getpc_b64 s[6:7]
	v_mbcnt_lo_u32_b32 v250, -1, 0
	v_mbcnt_hi_u32_b32 v250, -1, v250
	s_sub_u32 s0, s98, 4
	s_mul_i32 s0, s0, 0x2000
	s_add_u32 s6, s6, s0
	s_addc_u32 s7, s7, 0
	v_lshlrev_b32_e32 v250, 7, v250
	global_load_dword v251, v250, s[6:7]
.Lipf_skip_0:
	s_waitcnt lgkmcnt(0)
	s_mov_b32 s0, s98
	v_mbcnt_lo_u32_b32 v0, -1, 0
	v_mbcnt_hi_u32_b32 v0, -1, v0
	s_nop 1
	v_lshl_add_u32 v0, s0, 6, v0
	s_nop 0
	v_cmp_eq_u32_e32 vcc, 0, v0
	s_and_saveexec_b64 s[6:7], vcc
	s_cbranch_execz .LBB0_119
	s_add_i32 s0, 0, 0x24800
	v_mov_b32_e32 v0, s0
	s_waitcnt vmcnt(0) expcnt(0) lgkmcnt(0)
	ds_read_b32 v1, v0
	s_add_i32 s0, 0, 0x24804
	v_mov_b32_e32 v0, s0
	ds_read_b32 v0, v0
	s_waitcnt lgkmcnt(1)
	v_cmp_ne_u32_e32 vcc, 0, v1
	s_cbranch_vccz .Lcensus_0

.LBB0_381:
	s_cmp_gt_i32 s29, 3
	s_cselect_b64 s[4:5], -1, 0
	s_and_b64 s[0:1], s[6:7], s[4:5]
	s_andn2_b64 vcc, exec, s[0:1]
	s_cbranch_vccnz .LBB0_531
	s_waitcnt vmcnt(0)
	s_waitcnt lgkmcnt(0)
	s_barrier
	s_cmp_lt_u32 s98, 4
	s_cbranch_scc1 .Lipf_skip_1
	s_getpc_b64 s[6:7]
	v_mbcnt_lo_u32_b32 v250, -1, 0
	v_mbcnt_hi_u32_b32 v250, -1, v250
	s_sub_u32 s0, s98, 4
	s_mul_i32 s0, s0, 0x2000
	s_add_u32 s6, s6, s0
	s_addc_u32 s7, s7, 0
	v_lshlrev_b32_e32 v250, 7, v250
	global_load_dword v251, v250, s[6:7]

.LBB0_561:
	v_readlane_b32 s4, v249, 51
	v_readlane_b32 s5, v249, 52
	v_readlane_b32 s6, v249, 53
	v_readlane_b32 s7, v249, 54
	s_cmp_gt_i32 s5, 4
	s_cselect_b64 s[6:7], -1, 0
	s_and_b64 s[0:1], s[84:85], s[6:7]
	s_andn2_b64 vcc, exec, s[0:1]
	s_cbranch_vccnz .LBB0_711
	s_waitcnt vmcnt(0)
	s_waitcnt lgkmcnt(0)
	s_barrier
	s_cmp_lt_u32 s98, 4
	s_cbranch_scc1 .Lipf_skip_2
	s_getpc_b64 s[4:5]
	v_mbcnt_lo_u32_b32 v250, -1, 0
	v_mbcnt_hi_u32_b32 v250, -1, v250
	s_sub_u32 s0, s98, 4
	s_mul_i32 s0, s0, 0x2000
	s_add_u32 s4, s4, s0
	s_addc_u32 s5, s5, 0
	v_lshlrev_b32_e32 v250, 7, v250
	global_load_dword v251, v250, s[4:5]
.Lipf_skip_2:
	s_waitcnt lgkmcnt(0)
	s_mov_b32 s0, s98
	v_mbcnt_lo_u32_b32 v0, -1, 0
	v_mbcnt_hi_u32_b32 v0, -1, v0
	s_nop 1
	v_lshl_add_u32 v0, s0, 6, v0
	s_nop 0
	v_cmp_eq_u32_e32 vcc, 0, v0
	s_and_saveexec_b64 s[4:5], vcc
	s_cbranch_execz .LBB0_590
	s_add_i32 s0, 0, 0x24800
	v_mov_b32_e32 v0, s0
	s_waitcnt vmcnt(0) expcnt(0) lgkmcnt(0)
	ds_read_b32 v1, v0
	s_add_i32 s0, 0, 0x24804
	v_mov_b32_e32 v0, s0
	ds_read_b32 v0, v0
	s_waitcnt lgkmcnt(1)
	v_cmp_ne_u32_e32 vcc, 0, v1
	s_cbranch_vccz .Lcensus_2

.LBB0_732:
	s_cmp_gt_i32 s41, 5
	s_cselect_b64 s[12:13], -1, 0
	s_and_b64 s[0:1], s[8:9], s[12:13]
	s_andn2_b64 vcc, exec, s[0:1]
	s_cbranch_vccnz .LBB0_890
	s_waitcnt vmcnt(0)
	s_waitcnt lgkmcnt(0)
	s_barrier
	s_cmp_lt_u32 s98, 4
	s_cbranch_scc1 .Lipf_skip_3
	s_getpc_b64 s[6:7]
	v_mbcnt_lo_u32_b32 v250, -1, 0
	v_mbcnt_hi_u32_b32 v250, -1, v250
	s_sub_u32 s0, s98, 4
	s_mul_i32 s0, s0, 0x2000
	s_add_u32 s6, s6, s0
	s_addc_u32 s7, s7, 0
	v_lshlrev_b32_e32 v250, 7, v250
	global_load_dword v251, v250, s[6:7]

.LBB0_923:
	s_cmp_gt_i32 s41, 6
	s_cselect_b64 s[4:5], -1, 0
	s_and_b64 s[0:1], s[14:15], s[4:5]
	s_andn2_b64 vcc, exec, s[0:1]
	s_cbranch_vccnz .LBB0_1075
	s_waitcnt vmcnt(0)
	s_waitcnt lgkmcnt(0)
	s_barrier
	s_cmp_lt_u32 s98, 4
	s_cbranch_scc1 .Lipf_skip_4
	s_getpc_b64 s[12:13]
	v_mbcnt_lo_u32_b32 v250, -1, 0
	v_mbcnt_hi_u32_b32 v250, -1, v250
	s_sub_u32 s0, s98, 4
	s_mul_i32 s0, s0, 0x2000
	s_add_u32 s12, s12, s0
	s_addc_u32 s13, s13, 0
	v_lshlrev_b32_e32 v250, 7, v250
	global_load_dword v251, v250, s[12:13]
.Lipf_skip_4:
	s_waitcnt lgkmcnt(0)
	s_mov_b32 s0, s98
	v_mbcnt_lo_u32_b32 v0, -1, 0
	v_mbcnt_hi_u32_b32 v0, -1, v0
	s_nop 1
	v_lshl_add_u32 v0, s0, 6, v0
	s_nop 0
	v_cmp_eq_u32_e32 vcc, 0, v0
	s_and_saveexec_b64 s[12:13], vcc
	s_cbranch_execz .LBB0_954
	s_add_i32 s0, 0, 0x24800
	v_mov_b32_e32 v0, s0
	s_waitcnt vmcnt(0) expcnt(0) lgkmcnt(0)
	ds_read_b32 v1, v0
	s_add_i32 s0, 0, 0x24804
	v_mov_b32_e32 v0, s0
	ds_read_b32 v0, v0
	s_waitcnt lgkmcnt(1)
	v_cmp_ne_u32_e32 vcc, 0, v1
	s_cbranch_vccz .Lcensus_4

.LBB0_1440:
	v_readlane_b32 s48, v249, 51
	v_readlane_b32 s49, v249, 52
	s_cmp_lt_i32 s48, 8
	s_cselect_b64 s[0:1], -1, 0
	s_cmp_gt_i32 s49, 8
	s_cselect_b64 s[4:5], -1, 0
	s_and_b64 s[0:1], s[0:1], s[4:5]
	s_andn2_b64 vcc, exec, s[0:1]
	v_readlane_b32 s50, v249, 53
	v_readlane_b32 s51, v249, 54
	s_cbranch_vccnz .LBB0_1590
	s_waitcnt vmcnt(0)
	s_waitcnt vmcnt(0) lgkmcnt(0)
	s_barrier
	s_cmp_lt_u32 s98, 4
	s_cbranch_scc1 .Lipf_skip_5
	s_getpc_b64 s[6:7]
	v_mbcnt_lo_u32_b32 v250, -1, 0
	v_mbcnt_hi_u32_b32 v250, -1, v250
	s_sub_u32 s0, s98, 4
	s_mul_i32 s0, s0, 0x2000
	s_add_u32 s6, s6, s0
	s_addc_u32 s7, s7, 0
	v_lshlrev_b32_e32 v250, 7, v250
	global_load_dword v251, v250, s[6:7]

.LBB0_1603:
	s_cmp_gt_i32 s49, 9
	s_cselect_b64 s[4:5], -1, 0
	s_and_b64 s[0:1], s[6:7], s[4:5]
	s_andn2_b64 vcc, exec, s[0:1]
	s_cbranch_vccnz .LBB0_1753
	s_waitcnt vmcnt(0)
	s_waitcnt vmcnt(0) lgkmcnt(0)
	s_barrier
	s_cmp_lt_u32 s98, 4
	s_cbranch_scc1 .Lipf_skip_6
	s_getpc_b64 s[6:7]
	v_mbcnt_lo_u32_b32 v250, -1, 0
	v_mbcnt_hi_u32_b32 v250, -1, v250
	s_sub_u32 s0, s98, 4
	s_mul_i32 s0, s0, 0x2000
	s_add_u32 s6, s6, s0
	s_addc_u32 s7, s7, 0
	v_lshlrev_b32_e32 v250, 7, v250
	global_load_dword v251, v250, s[6:7]

.LBB0_1808:
	s_cmp_gt_i32 s49, 10
	s_cselect_b64 s[4:5], -1, 0
	s_and_b64 s[0:1], s[10:11], s[4:5]
	s_andn2_b64 vcc, exec, s[0:1]
	s_cbranch_vccnz .LBB0_1958
	s_waitcnt vmcnt(0)
	s_waitcnt vmcnt(0) lgkmcnt(0)
	s_barrier
	s_cmp_lt_u32 s98, 4
	s_cbranch_scc1 .Lipf_skip_7
	s_getpc_b64 s[6:7]
	v_mbcnt_lo_u32_b32 v250, -1, 0
	v_mbcnt_hi_u32_b32 v250, -1, v250
	s_sub_u32 s0, s98, 4
	s_mul_i32 s0, s0, 0x2000
	s_add_u32 s6, s6, s0
	s_addc_u32 s7, s7, 0
	v_lshlrev_b32_e32 v250, 7, v250
	global_load_dword v251, v250, s[6:7]

.LBB0_1973:
	s_cmp_gt_i32 s49, 11
	s_cselect_b64 s[6:7], -1, 0
	s_and_b64 s[0:1], s[10:11], s[6:7]
	s_andn2_b64 vcc, exec, s[0:1]
	s_cbranch_vccnz .LBB0_2123
	s_waitcnt vmcnt(0)
	s_waitcnt vmcnt(0) lgkmcnt(0)
	s_barrier
	s_cmp_lt_u32 s98, 4
	s_cbranch_scc1 .Lipf_skip_8
	s_getpc_b64 s[4:5]
	v_mbcnt_lo_u32_b32 v250, -1, 0
	v_mbcnt_hi_u32_b32 v250, -1, v250
	s_sub_u32 s0, s98, 4
	s_mul_i32 s0, s0, 0x2000
	s_add_u32 s4, s4, s0
	s_addc_u32 s5, s5, 0
	v_lshlrev_b32_e32 v250, 7, v250
	global_load_dword v251, v250, s[4:5]

.LBB0_2144:
	s_cmp_gt_i32 s49, 12
	s_cselect_b64 s[12:13], -1, 0
	s_and_b64 s[0:1], s[10:11], s[12:13]
	s_andn2_b64 vcc, exec, s[0:1]
	s_cbranch_vccnz .LBB0_2302
	s_waitcnt vmcnt(0)
	s_waitcnt vmcnt(0) lgkmcnt(0)
	s_barrier
	s_cmp_lt_u32 s98, 4
	s_cbranch_scc1 .Lipf_skip_9
	s_getpc_b64 s[6:7]
	v_mbcnt_lo_u32_b32 v250, -1, 0
	v_mbcnt_hi_u32_b32 v250, -1, v250
	s_sub_u32 s0, s98, 4
	s_mul_i32 s0, s0, 0x2000
	s_add_u32 s6, s6, s0
	s_addc_u32 s7, s7, 0
	v_lshlrev_b32_e32 v250, 7, v250
	global_load_dword v251, v250, s[6:7]

.LBB0_2335:
	s_cmp_gt_i32 s49, 13
	s_cselect_b64 s[4:5], -1, 0
	s_and_b64 s[0:1], s[14:15], s[4:5]
	s_andn2_b64 vcc, exec, s[0:1]
	s_cbranch_vccnz .LBB0_2397
	s_waitcnt vmcnt(0)
	s_waitcnt vmcnt(0) lgkmcnt(0)
	s_barrier
	s_cmp_lt_u32 s98, 4
	s_cbranch_scc1 .Lipf_skip_10
	s_getpc_b64 s[12:13]
	v_mbcnt_lo_u32_b32 v250, -1, 0
	v_mbcnt_hi_u32_b32 v250, -1, v250
	s_sub_u32 s0, s98, 4
	s_mul_i32 s0, s0, 0x2000
	s_add_u32 s12, s12, s0
	s_addc_u32 s13, s13, 0
	v_lshlrev_b32_e32 v250, 7, v250
	global_load_dword v251, v250, s[12:13]

.LBB0_2762:
	v_readlane_b32 s4, v249, 51
	v_readlane_b32 s5, v249, 52
	s_mov_b64 s[44:45], s[4:5]
	s_cmp_lt_i32 s44, 15
	v_readlane_b32 s6, v249, 53
	v_readlane_b32 s7, v249, 54
	s_cselect_b64 s[0:1], -1, 0
	s_cmp_gt_i32 s45, 15
	s_cselect_b64 s[6:7], -1, 0
	s_and_b64 s[0:1], s[0:1], s[6:7]
	s_andn2_b64 vcc, exec, s[0:1]
	s_cbranch_vccnz .LBB0_2822
	s_waitcnt vmcnt(0)
	s_waitcnt vmcnt(0) lgkmcnt(0)
	s_barrier
	s_cmp_lt_u32 s98, 4
	s_cbranch_scc1 .Lipf_skip_11
	s_getpc_b64 s[4:5]
	v_mbcnt_lo_u32_b32 v250, -1, 0
	v_mbcnt_hi_u32_b32 v250, -1, v250
	s_sub_u32 s0, s98, 4
	s_mul_i32 s0, s0, 0xc00
	s_add_u32 s4, s4, s0
	s_addc_u32 s5, s5, 0
	v_lshlrev_b32_e32 v250, 7, v250
	v_min_u32_e32 v250, 0xb80, v250
	global_load_dword v251, v250, s[4:5]

.LBB0_2866:
	s_cmp_gt_i32 s45, 16
	s_cselect_b64 s[0:1], -1, 0
	s_and_b64 s[0:1], s[4:5], s[0:1]
	s_andn2_b64 vcc, exec, s[0:1]
	s_cbranch_vccnz .LBB0_2926
	s_waitcnt vmcnt(0)
	s_waitcnt vmcnt(0) lgkmcnt(0)
	s_barrier
	s_cmp_lt_u32 s98, 4
	s_cbranch_scc1 .Lipf_skip_12
	s_getpc_b64 s[2:3]
	v_mbcnt_lo_u32_b32 v250, -1, 0
	v_mbcnt_hi_u32_b32 v250, -1, v250
	s_sub_u32 s0, s98, 4
	s_mul_i32 s0, s0, 0x200
	s_add_u32 s2, s2, s0
	s_addc_u32 s3, s3, 0
	v_lshlrev_b32_e32 v250, 7, v250
	v_min_u32_e32 v250, 0x180, v250
	global_load_dword v251, v250, s[2:3]
.Lipf_skip_12:
	s_waitcnt lgkmcnt(0)
	s_mov_b32 s0, s98
	v_mbcnt_lo_u32_b32 v0, -1, 0
	v_mbcnt_hi_u32_b32 v0, -1, v0
	s_nop 1
	v_lshl_add_u32 v0, s0, 6, v0
	s_nop 0
	v_cmp_eq_u32_e32 vcc, 0, v0
	s_and_saveexec_b64 s[2:3], vcc
	s_cbranch_execz .LBB0_2895
	s_add_i32 s0, 0, 0x24800
	v_mov_b32_e32 v0, s0
	s_waitcnt vmcnt(0) expcnt(0) lgkmcnt(0)
	ds_read_b32 v1, v0
	s_add_i32 s0, 0, 0x24804
	v_mov_b32_e32 v0, s0
	ds_read_b32 v0, v0
	s_waitcnt lgkmcnt(1)
	v_cmp_ne_u32_e32 vcc, 0, v1
	s_cbranch_vccz .Lcensus_12

	.amdhsa_kernel _Z4mega5MArgs
		.amdhsa_group_segment_fixed_size 0
		.amdhsa_private_segment_fixed_size 0
		.amdhsa_kernarg_size 496
		.amdhsa_user_sgpr_count 2
		.amdhsa_user_sgpr_dispatch_ptr 0
		.amdhsa_user_sgpr_queue_ptr 0
		.amdhsa_user_sgpr_kernarg_segment_ptr 1
		.amdhsa_user_sgpr_dispatch_id 0
		.amdhsa_user_sgpr_kernarg_preload_length 0
		.amdhsa_user_sgpr_kernarg_preload_offset 0
		.amdhsa_user_sgpr_private_segment_size 0
		.amdhsa_uses_dynamic_stack 0
		.amdhsa_enable_private_segment 0
		.amdhsa_system_sgpr_workgroup_id_x 1
		.amdhsa_system_sgpr_workgroup_id_y 0
		.amdhsa_system_sgpr_workgroup_id_z 0
		.amdhsa_system_sgpr_workgroup_info 0
		.amdhsa_system_vgpr_workitem_id 0
		.amdhsa_next_free_vgpr 252
		.amdhsa_next_free_sgpr 100
		.amdhsa_accum_offset 252
		.amdhsa_reserve_vcc 1
		.amdhsa_float_round_mode_32 0
		.amdhsa_float_round_mode_16_64 0
		.amdhsa_float_denorm_mode_32 3
		.amdhsa_float_denorm_mode_16_64 3
		.amdhsa_dx10_clamp 1
		.amdhsa_ieee_mode 1
		.amdhsa_fp16_overflow 0
		.amdhsa_tg_split 0
		.amdhsa_exception_fp_ieee_invalid_op 0
		.amdhsa_exception_fp_denorm_src 0
		.amdhsa_exception_fp_ieee_div_zero 0
		.amdhsa_exception_fp_ieee_overflow 0
		.amdhsa_exception_fp_ieee_underflow 0
		.amdhsa_exception_fp_ieee_inexact 0
		.amdhsa_exception_int_div_zero 0
	.end_amdhsa_kernel

amdhsa.kernels:
  - .agpr_count:     0
    .args:
      - .offset:         0
        .size:           240
        .value_kind:     by_value
      - .offset:         240
        .size:           4
        .value_kind:     hidden_block_count_x
      - .offset:         244
        .size:           4
        .value_kind:     hidden_block_count_y
      - .offset:         248
        .size:           4
        .value_kind:     hidden_block_count_z
      - .offset:         252
        .size:           2
        .value_kind:     hidden_group_size_x
      - .offset:         254
        .size:           2
        .value_kind:     hidden_group_size_y
      - .offset:         256
        .size:           2
        .value_kind:     hidden_group_size_z
      - .offset:         258
        .size:           2
        .value_kind:     hidden_remainder_x
      - .offset:         260
        .size:           2
        .value_kind:     hidden_remainder_y
      - .offset:         262
        .size:           2
        .value_kind:     hidden_remainder_z
      - .offset:         280
        .size:           8
        .value_kind:     hidden_global_offset_x
      - .offset:         288
        .size:           8
        .value_kind:     hidden_global_offset_y
      - .offset:         296
        .size:           8
        .value_kind:     hidden_global_offset_z
      - .offset:         304
        .size:           2
        .value_kind:     hidden_grid_dims
      - .offset:         360
        .size:           4
        .value_kind:     hidden_dynamic_lds_size
    .group_segment_fixed_size: 0
    .kernarg_segment_align: 8
    .kernarg_segment_size: 496
    .language:       OpenCL C
    .language_version:
      - 2
      - 0
    .max_flat_workgroup_size: 512
    .name:           _Z4mega5MArgs
    .private_segment_fixed_size: 0
    .sgpr_count:     106
    .sgpr_spill_count: 65
    .symbol:         _Z4mega5MArgs.kd
    .uniform_work_group_size: 1
    .uses_dynamic_stack: false
    .vgpr_count:     252
    .vgpr_spill_count: 0
    .wavefront_size: 64
